# grid barrier: leader bumps the XCD generation before its own invalidate; P10 combine loop handles two tokens per trip
# speedup vs baseline: 1.0018x; 1.0018x over previous
; __device__ __forceinline__ unsigned xb_ld(unsigned* p)              { return __hip_atomic_load(p, __ATOMIC_RELAXED, __HIP_MEMORY_SCOPE_AGENT); }
; __device__ __forceinline__ unsigned xb_add(unsigned* p, unsigned v) { return __hip_atomic_fetch_add(p, v, __ATOMIC_RELAXED, __HIP_MEMORY_SCOPE_AGENT); }
; #define XB_SPIN(cond, bar) do { unsigned _sp = 0; while (cond) { __builtin_amdgcn_s_sleep(1); \
;     if ((++_sp & 255u) == 0u) { if (xb_ld(&(bar)[XB_TMO])) break; if (_sp > XB_SPIN_CAP) { atomicAdd(&(bar)[XB_TMO], 1u); break; } } } } while (0)
; __device__ __forceinline__ void xcd_barrier(const XcdBarrier& b) {
;     ...
;             __builtin_amdgcn_fence(__ATOMIC_RELEASE, "agent");
;             asm volatile("s_waitcnt vmcnt(0)" ::: "memory");
;             const unsigned og = xb_add(&bar[XB_TOP], 1u);
;             const unsigned tg = og / nx;
;             if (og + 1u == (tg + 1u) * nx) xb_add(&bar[XB_TOPGEN], 1u);
;             else XB_SPIN(xb_ld(&bar[XB_TOPGEN]) == tg, bar);
;             __builtin_amdgcn_fence(__ATOMIC_ACQUIRE, "agent");
;             xb_add(&bar[XB_XGEN(b.x)], 1u);
;             asm volatile("s_waitcnt vmcnt(0)" ::: "memory");
.LBB0_198:
	s_or_b64 exec, exec, s[4:5]
	v_mov_b32_e32 v1, 0x2000
	v_mov_b32_e32 v2, 1
	s_waitcnt vmcnt(0)
	global_atomic_add v1, v2, s[0:1] offset:1024
	buffer_inv sc1
	s_waitcnt vmcnt(0)

; __device__ __forceinline__ unsigned xb_ld(unsigned* p)              { return __hip_atomic_load(p, __ATOMIC_RELAXED, __HIP_MEMORY_SCOPE_AGENT); }
; __device__ __forceinline__ unsigned xb_add(unsigned* p, unsigned v) { return __hip_atomic_fetch_add(p, v, __ATOMIC_RELAXED, __HIP_MEMORY_SCOPE_AGENT); }
; #define XB_SPIN(cond, bar) do { unsigned _sp = 0; while (cond) { __builtin_amdgcn_s_sleep(1); \
;     if ((++_sp & 255u) == 0u) { if (xb_ld(&(bar)[XB_TMO])) break; if (_sp > XB_SPIN_CAP) { atomicAdd(&(bar)[XB_TMO], 1u); break; } } } } while (0)
; __device__ __forceinline__ void xcd_barrier(const XcdBarrier& b) {
;     ...
;             __builtin_amdgcn_fence(__ATOMIC_RELEASE, "agent");
;             asm volatile("s_waitcnt vmcnt(0)" ::: "memory");
;             const unsigned og = xb_add(&bar[XB_TOP], 1u);
;             const unsigned tg = og / nx;
;             if (og + 1u == (tg + 1u) * nx) xb_add(&bar[XB_TOPGEN], 1u);
;             else XB_SPIN(xb_ld(&bar[XB_TOPGEN]) == tg, bar);
;             __builtin_amdgcn_fence(__ATOMIC_ACQUIRE, "agent");
;             xb_add(&bar[XB_XGEN(b.x)], 1u);
;             asm volatile("s_waitcnt vmcnt(0)" ::: "memory");
.LBB0_312:
	s_or_b64 exec, exec, s[4:5]
	v_mov_b32_e32 v1, 0x2000
	v_mov_b32_e32 v2, 1
	s_waitcnt vmcnt(0)
	global_atomic_add v1, v2, s[2:3] offset:1024
	buffer_inv sc1
	s_waitcnt vmcnt(0)

; #define GAS __attribute__((address_space(1)))
; __device__ __forceinline__ void p10_final(Frame& F, const Args& A) {
;     ...
;     for (int t = gw; t < T; t += NGW) {
;         float v[16];
;         const int4 pi = *(const int4*)(pinf + 4 * t); const f32x4 pw4 = *(const f32x4*)(pwt + 4 * t);
;         const int pinfo4[4] = {pi.x, pi.y, pi.z, pi.w};
; #pragma unroll
;         for (int j = 0; j < 4; ++j) { const u32x2 w = *(const GAS u32x2*)(x2b + (size_t)t * D + 256 * j + 4 * lane);
;             v[4 * j] = bflo(w.x); v[4 * j + 1] = bfhi(w.x); v[4 * j + 2] = bflo(w.y); v[4 * j + 3] = bfhi(w.y); }
; #pragma unroll
;         for (int k = 0; k < 4; ++k) { const int e = pinfo4[k] & 31, pos = pinfo4[k] >> 5; const size_t row = (size_t)tpre[e] * 256 + pos; const float wk = pw4[k];
; #pragma unroll
;             for (int j = 0; j < 4; ++j) { const unsigned w = *(const GAS unsigned*)(Y + row * D + 256 * j + 4 * lane);
;                 const f32x2 a0 = __builtin_amdgcn_cvt_pk_f32_fp8((int)w, false), a1 = __builtin_amdgcn_cvt_pk_f32_fp8((int)w, true);
;                 v[4 * j] += wk * a0[0]; v[4 * j + 1] += wk * a0[1]; v[4 * j + 2] += wk * a1[0]; v[4 * j + 3] += wk * a1[1]; } }
.LBB0_1146:
	s_ashr_i32 s7, s6, 31
	s_lshl_b64 s[18:19], s[6:7], 2
	s_add_u32 s20, s12, s18
	s_addc_u32 s21, s13, s19
	s_add_u32 s18, s14, s18
	global_load_dwordx2 v[22:23], v[20:21], off offset:1024
	global_load_dwordx2 v[28:29], v[20:21], off offset:1536
	global_load_dwordx2 v[26:27], v[20:21], off
	global_load_dwordx2 v[24:25], v[20:21], off offset:512
	s_addc_u32 s19, s15, s19
	global_load_dwordx4 v[32:35], v19, s[20:21]
	global_load_dwordx4 v[36:39], v19, s[18:19]
	s_add_i32 s30, s6, s16
	v_lshl_add_u64 v[120:121], v[20:21], 0, s[10:11]
	s_ashr_i32 s31, s30, 31
	s_lshl_b64 s[36:37], s[30:31], 2
	s_add_u32 s38, s12, s36
	s_addc_u32 s39, s13, s37
	s_add_u32 s36, s14, s36
	global_load_dwordx2 v[122:123], v[120:121], off offset:1024
	global_load_dwordx2 v[128:129], v[120:121], off offset:1536
	global_load_dwordx2 v[126:127], v[120:121], off
	global_load_dwordx2 v[124:125], v[120:121], off offset:512
	s_addc_u32 s37, s15, s37
	global_load_dwordx4 v[132:135], v19, s[38:39]
	global_load_dwordx4 v[136:139], v19, s[36:37]
	s_add_i32 s0, s0, s2
	s_add_i32 s0, s0, s2
	s_add_i32 s6, s30, s16
	v_lshl_add_u64 v[20:21], v[120:121], 0, s[10:11]
	v_lshl_add_u64 v[118:119], v[0:1], 0, s[8:9]
	s_waitcnt vmcnt(7)
	v_and_b32_e32 v41, 0xffff0000, v23
	v_lshlrev_b32_e32 v40, 16, v23
	v_and_b32_e32 v43, 0xffff0000, v28
	v_lshlrev_b32_e32 v42, 16, v28
	v_readfirstlane_b32 s20, v32
	v_readfirstlane_b32 s7, v35
	v_readfirstlane_b32 s17, v34
	v_readfirstlane_b32 s19, v33
	s_and_b32 s21, s20, 31
	s_and_b32 s23, s19, 31
	s_ashr_i32 s22, s17, 5
	s_and_b32 s17, s17, 31
	s_ashr_i32 s24, s7, 5
	s_and_b32 s7, s7, 31
	s_lshl_b32 s26, s21, 2
	s_lshl_b32 s27, s23, 2
	s_lshl_b32 s17, s17, 2
	s_lshl_b32 s7, s7, 2
	s_add_i32 s26, s1, s26
	s_add_i32 s27, s1, s27
	s_add_i32 s17, s1, s17
	s_add_i32 s7, s1, s7
	v_mov_b32_e32 v23, s26
	v_mov_b32_e32 v31, s27
	v_mov_b32_e32 v33, s17
	v_mov_b32_e32 v35, s7
	ds_read_b32 v32, v23
	ds_read_b32 v34, v31
	ds_read_b32 v50, v33
	ds_read_b32 v52, v35
	s_ashr_i32 s18, s20, 5
	s_waitcnt lgkmcnt(3)
	v_ashrrev_i32_e32 v33, 31, v32
	s_ashr_i32 s20, s19, 5
	s_ashr_i32 s19, s18, 31
	s_waitcnt lgkmcnt(2)
	v_ashrrev_i32_e32 v35, 31, v34
	s_waitcnt lgkmcnt(1)
	v_ashrrev_i32_e32 v51, 31, v50
	s_waitcnt lgkmcnt(0)
	v_ashrrev_i32_e32 v53, 31, v52
	v_lshlrev_b64 v[32:33], 18, v[32:33]
	s_ashr_i32 s21, s20, 31
	s_ashr_i32 s23, s22, 31
	s_ashr_i32 s25, s24, 31
	s_lshl_b64 s[18:19], s[18:19], 10
	v_lshlrev_b64 v[34:35], 18, v[34:35]
	v_lshlrev_b64 v[50:51], 18, v[50:51]
	v_lshlrev_b64 v[52:53], 18, v[52:53]
	v_lshl_add_u64 v[32:33], s[4:5], 0, v[32:33]
	s_lshl_b64 s[20:21], s[20:21], 10
	s_lshl_b64 s[22:23], s[22:23], 10
	s_lshl_b64 s[24:25], s[24:25], 10
	v_lshl_add_u64 v[34:35], s[4:5], 0, v[34:35]
	v_lshl_add_u64 v[50:51], s[4:5], 0, v[50:51]
	v_lshl_add_u64 v[52:53], s[4:5], 0, v[52:53]
	v_lshl_add_u64 v[32:33], v[32:33], 0, s[18:19]
	v_lshl_add_u64 v[34:35], v[34:35], 0, s[20:21]
	v_lshl_add_u64 v[50:51], v[50:51], 0, s[22:23]
	v_lshl_add_u64 v[52:53], v[52:53], 0, s[24:25]
	v_lshl_add_u64 v[32:33], v[32:33], 0, v[18:19]
	v_lshl_add_u64 v[34:35], v[34:35], 0, v[18:19]
	v_lshl_add_u64 v[50:51], v[50:51], 0, v[18:19]
	v_lshl_add_u64 v[52:53], v[52:53], 0, v[18:19]
	global_load_dword v23, v[32:33], off
	global_load_dword v31, v[32:33], off offset:256
	global_load_dword v56, v[32:33], off offset:512
	global_load_dword v60, v[32:33], off offset:768
	global_load_dword v64, v[34:35], off
	global_load_dword v68, v[34:35], off offset:256
	global_load_dword v72, v[34:35], off offset:512
	global_load_dword v76, v[34:35], off offset:768
	global_load_dword v80, v[50:51], off
	global_load_dword v84, v[50:51], off offset:256
	global_load_dword v88, v[50:51], off offset:512
	global_load_dword v92, v[50:51], off offset:768
	global_load_dword v96, v[52:53], off
	global_load_dword v100, v[52:53], off offset:256
	global_load_dword v104, v[52:53], off offset:512
	global_load_dword v108, v[52:53], off offset:768
	s_waitcnt vmcnt(17)
	v_and_b32_e32 v141, 0xffff0000, v123
	v_lshlrev_b32_e32 v140, 16, v123
	v_and_b32_e32 v143, 0xffff0000, v128
	v_lshlrev_b32_e32 v142, 16, v128
	v_readfirstlane_b32 s38, v132
	v_readfirstlane_b32 s31, v135
	v_readfirstlane_b32 s28, v134
	v_readfirstlane_b32 s37, v133
	s_and_b32 s39, s38, 31
	s_and_b32 s41, s37, 31
	s_ashr_i32 s40, s28, 5
	s_and_b32 s28, s28, 31
	s_ashr_i32 s42, s31, 5
	s_and_b32 s31, s31, 31
	s_lshl_b32 s44, s39, 2
	s_lshl_b32 s45, s41, 2
	s_lshl_b32 s28, s28, 2
	s_lshl_b32 s31, s31, 2
	s_add_i32 s44, s1, s44
	s_add_i32 s45, s1, s45
	s_add_i32 s28, s1, s28
	s_add_i32 s31, s1, s31
	v_mov_b32_e32 v123, s44
	v_mov_b32_e32 v131, s45
	v_mov_b32_e32 v133, s28
	v_mov_b32_e32 v135, s31
	ds_read_b32 v132, v123
	ds_read_b32 v134, v131
	ds_read_b32 v150, v133
	ds_read_b32 v152, v135
	s_ashr_i32 s36, s38, 5
	s_waitcnt lgkmcnt(3)
	v_ashrrev_i32_e32 v133, 31, v132
	s_ashr_i32 s38, s37, 5
	s_ashr_i32 s37, s36, 31
	s_waitcnt lgkmcnt(2)
	v_ashrrev_i32_e32 v135, 31, v134
	s_waitcnt lgkmcnt(1)
	v_ashrrev_i32_e32 v151, 31, v150
	s_waitcnt lgkmcnt(0)
; #define GAS __attribute__((address_space(1)))
; __device__ __forceinline__ void p10_final(Frame& F, const Args& A) {
;     ...
;         for (int k = 0; k < 4; ++k) { const int e = pinfo4[k] & 31, pos = pinfo4[k] >> 5; const size_t row = (size_t)tpre[e] * 256 + pos; const float wk = pw4[k];
; #pragma unroll
;             for (int j = 0; j < 4; ++j) { const unsigned w = *(const GAS unsigned*)(Y + row * D + 256 * j + 4 * lane);
;                 const f32x2 a0 = __builtin_amdgcn_cvt_pk_f32_fp8((int)w, false), a1 = __builtin_amdgcn_cvt_pk_f32_fp8((int)w, true);
;                 v[4 * j] += wk * a0[0]; v[4 * j + 1] += wk * a0[1]; v[4 * j + 2] += wk * a1[0]; v[4 * j + 3] += wk * a1[1]; } }
;         float s = 0.f;
; #pragma unroll
;         for (int j = 0; j < 16; ++j) s += v[j] * v[j];
;         const float r = rsqrtf(wave_sum(s) * (1.0f / D) + EPS);
	v_ashrrev_i32_e32 v153, 31, v152
	v_lshlrev_b64 v[132:133], 18, v[132:133]
	s_ashr_i32 s39, s38, 31
	s_ashr_i32 s41, s40, 31
	s_ashr_i32 s43, s42, 31
	s_lshl_b64 s[36:37], s[36:37], 10
	v_lshlrev_b64 v[134:135], 18, v[134:135]
	v_lshlrev_b64 v[150:151], 18, v[150:151]
	v_lshlrev_b64 v[152:153], 18, v[152:153]
	v_lshl_add_u64 v[132:133], s[4:5], 0, v[132:133]
	s_lshl_b64 s[38:39], s[38:39], 10
	s_lshl_b64 s[40:41], s[40:41], 10
	s_lshl_b64 s[42:43], s[42:43], 10
	v_lshl_add_u64 v[134:135], s[4:5], 0, v[134:135]
	v_lshl_add_u64 v[150:151], s[4:5], 0, v[150:151]
	v_lshl_add_u64 v[152:153], s[4:5], 0, v[152:153]
	v_lshl_add_u64 v[132:133], v[132:133], 0, s[36:37]
	v_lshl_add_u64 v[134:135], v[134:135], 0, s[38:39]
	v_lshl_add_u64 v[150:151], v[150:151], 0, s[40:41]
	v_lshl_add_u64 v[152:153], v[152:153], 0, s[42:43]
	v_lshl_add_u64 v[132:133], v[132:133], 0, v[18:19]
	v_lshl_add_u64 v[134:135], v[134:135], 0, v[18:19]
	v_lshl_add_u64 v[150:151], v[150:151], 0, v[18:19]
	v_lshl_add_u64 v[152:153], v[152:153], 0, v[18:19]
	global_load_dword v123, v[132:133], off
	global_load_dword v131, v[132:133], off offset:256
	global_load_dword v156, v[132:133], off offset:512
	global_load_dword v160, v[132:133], off offset:768
	global_load_dword v164, v[134:135], off
	global_load_dword v168, v[134:135], off offset:256
	global_load_dword v172, v[134:135], off offset:512
	global_load_dword v176, v[134:135], off offset:768
	global_load_dword v180, v[150:151], off
	global_load_dword v184, v[150:151], off offset:256
	global_load_dword v188, v[150:151], off offset:512
	global_load_dword v192, v[150:151], off offset:768
	global_load_dword v196, v[152:153], off
	global_load_dword v200, v[152:153], off offset:256
	global_load_dword v204, v[152:153], off offset:512
	global_load_dword v208, v[152:153], off offset:768
	s_waitcnt vmcnt(16)
	v_and_b32_e32 v45, 0xffff0000, v29
	v_lshlrev_b32_e32 v44, 16, v29
	v_lshlrev_b32_e32 v28, 16, v26
	v_and_b32_e32 v29, 0xffff0000, v26
	v_lshlrev_b32_e32 v26, 16, v27
	v_and_b32_e32 v27, 0xffff0000, v27
	v_lshlrev_b32_e32 v46, 16, v24
	v_and_b32_e32 v47, 0xffff0000, v24
	v_lshlrev_b32_e32 v48, 16, v22
	v_and_b32_e32 v49, 0xffff0000, v22
	v_mov_b32_e32 v22, v39
	v_lshlrev_b32_e32 v24, 16, v25
	v_and_b32_e32 v25, 0xffff0000, v25
	v_cvt_pk_f32_fp8_e32 v[32:33], v23
	v_cvt_pk_f32_fp8_sdwa v[34:35], v23 src0_sel:WORD_1
	v_cvt_pk_f32_fp8_e32 v[50:51], v31
	v_cvt_pk_f32_fp8_sdwa v[52:53], v31 src0_sel:WORD_1
	v_cvt_pk_f32_fp8_e32 v[62:63], v64
	v_cvt_pk_f32_fp8_sdwa v[64:65], v64 src0_sel:WORD_1
	v_cvt_pk_f32_fp8_e32 v[66:67], v68
	v_pk_fma_f32 v[28:29], v[36:37], v[32:33], v[28:29] op_sel_hi:[0,1,1]
	v_cvt_pk_f32_fp8_e32 v[78:79], v80
	v_cvt_pk_f32_fp8_sdwa v[80:81], v80 src0_sel:WORD_1
	v_cvt_pk_f32_fp8_e32 v[54:55], v56
	v_cvt_pk_f32_fp8_e32 v[82:83], v84
	v_cvt_pk_f32_fp8_e32 v[94:95], v96
	v_cvt_pk_f32_fp8_sdwa v[96:97], v96 src0_sel:WORD_1
	v_pk_fma_f32 v[26:27], v[36:37], v[34:35], v[26:27] op_sel_hi:[0,1,1]
	v_pk_fma_f32 v[28:29], v[36:37], v[62:63], v[28:29] op_sel:[1,0,0]
	v_cvt_pk_f32_fp8_sdwa v[68:69], v68 src0_sel:WORD_1
	v_cvt_pk_f32_fp8_e32 v[98:99], v100
	v_pk_fma_f32 v[26:27], v[36:37], v[64:65], v[26:27] op_sel:[1,0,0]
	v_pk_fma_f32 v[28:29], v[38:39], v[78:79], v[28:29] op_sel_hi:[0,1,1]
	v_cvt_pk_f32_fp8_sdwa v[56:57], v56 src0_sel:WORD_1
	v_cvt_pk_f32_fp8_e32 v[58:59], v60
	v_cvt_pk_f32_fp8_sdwa v[60:61], v60 src0_sel:WORD_1
	v_cvt_pk_f32_fp8_sdwa v[84:85], v84 src0_sel:WORD_1
	v_pk_fma_f32 v[32:33], v[36:37], v[50:51], v[46:47] op_sel_hi:[0,1,1]
	v_pk_fma_f32 v[26:27], v[38:39], v[80:81], v[26:27] op_sel_hi:[0,1,1]
	v_pk_fma_f32 v[28:29], v[22:23], v[94:95], v[28:29] op_sel_hi:[0,1,1]
	v_cvt_pk_f32_fp8_e32 v[70:71], v72
	v_cvt_pk_f32_fp8_sdwa v[72:73], v72 src0_sel:WORD_1
	v_cvt_pk_f32_fp8_e32 v[74:75], v76
	v_cvt_pk_f32_fp8_sdwa v[76:77], v76 src0_sel:WORD_1
	v_cvt_pk_f32_fp8_sdwa v[100:101], v100 src0_sel:WORD_1
	v_pk_fma_f32 v[32:33], v[36:37], v[66:67], v[32:33] op_sel:[1,0,0]
	v_pk_fma_f32 v[26:27], v[22:23], v[96:97], v[26:27] op_sel_hi:[0,1,1]
	v_pk_mul_f32 v[46:47], v[28:29], v[28:29]
	v_cvt_pk_f32_fp8_e32 v[86:87], v88
	v_cvt_pk_f32_fp8_sdwa v[88:89], v88 src0_sel:WORD_1
	v_cvt_pk_f32_fp8_e32 v[90:91], v92
	v_cvt_pk_f32_fp8_sdwa v[92:93], v92 src0_sel:WORD_1
	v_pk_fma_f32 v[24:25], v[36:37], v[52:53], v[24:25] op_sel_hi:[0,1,1]
	v_pk_fma_f32 v[34:35], v[36:37], v[54:55], v[48:49] op_sel_hi:[0,1,1]
	v_pk_fma_f32 v[32:33], v[38:39], v[82:83], v[32:33] op_sel_hi:[0,1,1]
	v_pk_mul_f32 v[48:49], v[26:27], v[26:27]
	v_add_f32_e32 v31, v46, v47
	v_cvt_pk_f32_fp8_e32 v[102:103], v104
	v_cvt_pk_f32_fp8_sdwa v[104:105], v104 src0_sel:WORD_1
	v_cvt_pk_f32_fp8_e32 v[106:107], v108
	v_cvt_pk_f32_fp8_sdwa v[108:109], v108 src0_sel:WORD_1
	v_pk_fma_f32 v[24:25], v[36:37], v[68:69], v[24:25] op_sel:[1,0,0]
	v_pk_fma_f32 v[32:33], v[22:23], v[98:99], v[32:33] op_sel_hi:[0,1,1]
	v_add_f32_e32 v31, v31, v48
	v_pk_fma_f32 v[40:41], v[36:37], v[56:57], v[40:41] op_sel_hi:[0,1,1]
	v_pk_fma_f32 v[42:43], v[36:37], v[58:59], v[42:43] op_sel_hi:[0,1,1]
	v_pk_fma_f32 v[44:45], v[36:37], v[60:61], v[44:45] op_sel_hi:[0,1,1]
	v_pk_fma_f32 v[24:25], v[38:39], v[84:85], v[24:25] op_sel_hi:[0,1,1]
	v_pk_mul_f32 v[50:51], v[32:33], v[32:33]
	v_add_f32_e32 v31, v49, v31
	v_pk_fma_f32 v[40:41], v[36:37], v[72:73], v[40:41] op_sel:[1,0,0]
	v_pk_fma_f32 v[42:43], v[36:37], v[74:75], v[42:43] op_sel:[1,0,0]
	v_pk_fma_f32 v[44:45], v[36:37], v[76:77], v[44:45] op_sel:[1,0,0]
	v_pk_fma_f32 v[34:35], v[36:37], v[70:71], v[34:35] op_sel:[1,0,0]
	v_pk_fma_f32 v[24:25], v[22:23], v[100:101], v[24:25] op_sel_hi:[0,1,1]
	v_add_f32_e32 v31, v31, v50
; #define GAS __attribute__((address_space(1)))
; __device__ __forceinline__ void p10_final(Frame& F, const Args& A) {
;     ...
;         float s = 0.f;
; #pragma unroll
;         for (int j = 0; j < 16; ++j) s += v[j] * v[j];
;         const float r = rsqrtf(wave_sum(s) * (1.0f / D) + EPS);
; #pragma unroll
;         for (int j = 0; j < 4; ++j)
;             __builtin_nontemporal_store((f32x4){v[4 * j] * r * g[j][0], v[4 * j + 1] * r * g[j][1], v[4 * j + 2] * r * g[j][2], v[4 * j + 3] * r * g[j][3]}, (GAS f32x4*)(out + (size_t)t * D + 256 * j + 4 * lane));
	v_pk_fma_f32 v[36:37], v[38:39], v[88:89], v[40:41] op_sel_hi:[0,1,1]
	v_pk_fma_f32 v[40:41], v[38:39], v[90:91], v[42:43] op_sel_hi:[0,1,1]
	v_pk_fma_f32 v[42:43], v[38:39], v[92:93], v[44:45] op_sel_hi:[0,1,1]
	v_pk_fma_f32 v[34:35], v[38:39], v[86:87], v[34:35] op_sel_hi:[0,1,1]
	v_pk_mul_f32 v[52:53], v[24:25], v[24:25]
	v_add_f32_e32 v31, v51, v31
	v_pk_fma_f32 v[36:37], v[22:23], v[104:105], v[36:37] op_sel_hi:[0,1,1]
	v_pk_fma_f32 v[38:39], v[22:23], v[106:107], v[40:41] op_sel_hi:[0,1,1]
	v_pk_fma_f32 v[40:41], v[22:23], v[108:109], v[42:43] op_sel_hi:[0,1,1]
	v_pk_fma_f32 v[22:23], v[22:23], v[102:103], v[34:35] op_sel_hi:[0,1,1]
	v_add_f32_e32 v31, v52, v31
	v_pk_mul_f32 v[54:55], v[22:23], v[22:23]
	v_add_f32_e32 v31, v53, v31
	v_add_f32_e32 v31, v54, v31
	v_pk_mul_f32 v[34:35], v[36:37], v[36:37]
	v_add_f32_e32 v31, v55, v31
	v_add_f32_e32 v31, v34, v31
	v_pk_mul_f32 v[42:43], v[38:39], v[38:39]
	v_add_f32_e32 v31, v35, v31
	v_add_f32_e32 v31, v42, v31
	v_pk_mul_f32 v[44:45], v[40:41], v[40:41]
	v_add_f32_e32 v31, v43, v31
	v_add_f32_e32 v31, v44, v31
	v_add_f32_e32 v31, v45, v31
	s_nop 1
	v_add_f32_dpp v31, v31, v31 row_ror:1 row_mask:0xf bank_mask:0xf bound_ctrl:1
	s_nop 1
	v_add_f32_dpp v31, v31, v31 row_ror:2 row_mask:0xf bank_mask:0xf bound_ctrl:1
	s_nop 1
	v_add_f32_dpp v31, v31, v31 row_ror:4 row_mask:0xf bank_mask:0xf bound_ctrl:1
	s_nop 1
	v_add_f32_dpp v31, v31, v31 row_ror:8 row_mask:0xf bank_mask:0xf bound_ctrl:1
	s_nop 0
	v_readlane_b32 s7, v31, 16
	v_readlane_b32 s17, v31, 48
	v_readlane_b32 s18, v31, 0
	v_readlane_b32 s19, v31, 32
	v_mov_b32_e32 v34, s7
	v_mov_b32_e32 v35, s17
	v_pk_add_f32 v[34:35], s[18:19], v[34:35]
	s_nop 0
	v_add_f32_e32 v31, v34, v35
	v_fmamk_f32 v31, v31, 0x3a800000, v30
	v_mul_f32_e32 v34, 0x4b800000, v31
	v_cmp_gt_f32_e32 vcc, s3, v31
	s_nop 1
	v_cndmask_b32_e32 v31, v31, v34, vcc
	v_rsq_f32_e32 v31, v31
	s_nop 0
	v_mul_f32_e32 v34, 0x45800000, v31
	v_cndmask_b32_e32 v34, v31, v34, vcc
	v_pk_mul_f32 v[28:29], v[28:29], v[34:35] op_sel_hi:[1,0]
	v_pk_mul_f32 v[26:27], v[26:27], v[34:35] op_sel_hi:[1,0]
	v_pk_mul_f32 v[32:33], v[32:33], v[34:35] op_sel_hi:[1,0]
	v_pk_mul_f32 v[42:43], v[24:25], v[34:35] op_sel_hi:[1,0]
	v_pk_mul_f32 v[44:45], v[22:23], v[34:35] op_sel_hi:[1,0]
	v_pk_mul_f32 v[36:37], v[36:37], v[34:35] op_sel_hi:[1,0]
	v_pk_mul_f32 v[46:47], v[38:39], v[34:35] op_sel_hi:[1,0]
	v_pk_mul_f32 v[38:39], v[40:41], v[34:35] op_sel_hi:[1,0]
	v_pk_mul_f32 v[24:25], v[16:17], v[26:27]
	v_pk_mul_f32 v[22:23], v[14:15], v[28:29]
	v_pk_mul_f32 v[28:29], v[12:13], v[42:43]
	v_pk_mul_f32 v[26:27], v[10:11], v[32:33]
	v_pk_mul_f32 v[34:35], v[8:9], v[36:37]
	v_pk_mul_f32 v[32:33], v[6:7], v[44:45]
	v_pk_mul_f32 v[38:39], v[4:5], v[38:39]
	v_pk_mul_f32 v[36:37], v[2:3], v[46:47]
	global_store_dwordx4 v[0:1], v[22:25], off offset:-3072 nt
	global_store_dwordx4 v[0:1], v[26:29], off offset:-2048 nt
	global_store_dwordx4 v[0:1], v[32:35], off offset:-1024 nt
	global_store_dwordx4 v[0:1], v[36:39], off nt
	s_waitcnt vmcnt(4)
	v_and_b32_e32 v145, 0xffff0000, v129
	v_lshlrev_b32_e32 v144, 16, v129
	v_lshlrev_b32_e32 v128, 16, v126
	v_and_b32_e32 v129, 0xffff0000, v126
	v_lshlrev_b32_e32 v126, 16, v127
	v_and_b32_e32 v127, 0xffff0000, v127
	v_lshlrev_b32_e32 v146, 16, v124
	v_and_b32_e32 v147, 0xffff0000, v124
	v_lshlrev_b32_e32 v148, 16, v122
	v_and_b32_e32 v149, 0xffff0000, v122
	v_mov_b32_e32 v122, v139
	v_lshlrev_b32_e32 v124, 16, v125
	v_and_b32_e32 v125, 0xffff0000, v125
	v_cvt_pk_f32_fp8_e32 v[132:133], v123
	v_cvt_pk_f32_fp8_sdwa v[134:135], v123 src0_sel:WORD_1
	v_cvt_pk_f32_fp8_e32 v[150:151], v131
	v_cvt_pk_f32_fp8_sdwa v[152:153], v131 src0_sel:WORD_1
	v_cvt_pk_f32_fp8_e32 v[162:163], v164
	v_cvt_pk_f32_fp8_sdwa v[164:165], v164 src0_sel:WORD_1
	v_cvt_pk_f32_fp8_e32 v[166:167], v168
	v_pk_fma_f32 v[128:129], v[136:137], v[132:133], v[128:129] op_sel_hi:[0,1,1]
	v_cvt_pk_f32_fp8_e32 v[178:179], v180
	v_cvt_pk_f32_fp8_sdwa v[180:181], v180 src0_sel:WORD_1
	v_cvt_pk_f32_fp8_e32 v[154:155], v156
	v_cvt_pk_f32_fp8_e32 v[182:183], v184
	v_cvt_pk_f32_fp8_e32 v[194:195], v196
	v_cvt_pk_f32_fp8_sdwa v[196:197], v196 src0_sel:WORD_1
	v_pk_fma_f32 v[126:127], v[136:137], v[134:135], v[126:127] op_sel_hi:[0,1,1]
	v_pk_fma_f32 v[128:129], v[136:137], v[162:163], v[128:129] op_sel:[1,0,0]
	v_cvt_pk_f32_fp8_sdwa v[168:169], v168 src0_sel:WORD_1
	v_cvt_pk_f32_fp8_e32 v[198:199], v200
	v_pk_fma_f32 v[126:127], v[136:137], v[164:165], v[126:127] op_sel:[1,0,0]
	v_pk_fma_f32 v[128:129], v[138:139], v[178:179], v[128:129] op_sel_hi:[0,1,1]
	v_cvt_pk_f32_fp8_sdwa v[156:157], v156 src0_sel:WORD_1
	v_cvt_pk_f32_fp8_e32 v[158:159], v160
	v_cvt_pk_f32_fp8_sdwa v[160:161], v160 src0_sel:WORD_1
	v_cvt_pk_f32_fp8_sdwa v[184:185], v184 src0_sel:WORD_1
	v_pk_fma_f32 v[132:133], v[136:137], v[150:151], v[146:147] op_sel_hi:[0,1,1]
	v_pk_fma_f32 v[126:127], v[138:139], v[180:181], v[126:127] op_sel_hi:[0,1,1]
	v_pk_fma_f32 v[128:129], v[122:123], v[194:195], v[128:129] op_sel_hi:[0,1,1]
	v_cvt_pk_f32_fp8_e32 v[170:171], v172
	v_cvt_pk_f32_fp8_sdwa v[172:173], v172 src0_sel:WORD_1
	v_cvt_pk_f32_fp8_e32 v[174:175], v176
	v_cvt_pk_f32_fp8_sdwa v[176:177], v176 src0_sel:WORD_1
	v_cvt_pk_f32_fp8_sdwa v[200:201], v200 src0_sel:WORD_1
; #define GAS __attribute__((address_space(1)))
; __device__ __forceinline__ void p10_final(Frame& F, const Args& A) {
;     ...
;         for (int k = 0; k < 4; ++k) { const int e = pinfo4[k] & 31, pos = pinfo4[k] >> 5; const size_t row = (size_t)tpre[e] * 256 + pos; const float wk = pw4[k];
; #pragma unroll
;             for (int j = 0; j < 4; ++j) { const unsigned w = *(const GAS unsigned*)(Y + row * D + 256 * j + 4 * lane);
;                 const f32x2 a0 = __builtin_amdgcn_cvt_pk_f32_fp8((int)w, false), a1 = __builtin_amdgcn_cvt_pk_f32_fp8((int)w, true);
;                 v[4 * j] += wk * a0[0]; v[4 * j + 1] += wk * a0[1]; v[4 * j + 2] += wk * a1[0]; v[4 * j + 3] += wk * a1[1]; } }
;         float s = 0.f;
; #pragma unroll
;         for (int j = 0; j < 16; ++j) s += v[j] * v[j];
;         const float r = rsqrtf(wave_sum(s) * (1.0f / D) + EPS);
; #pragma unroll
;         for (int j = 0; j < 4; ++j)
;             __builtin_nontemporal_store((f32x4){v[4 * j] * r * g[j][0], v[4 * j + 1] * r * g[j][1], v[4 * j + 2] * r * g[j][2], v[4 * j + 3] * r * g[j][3]}, (GAS f32x4*)(out + (size_t)t * D + 256 * j + 4 * lane));
	v_pk_fma_f32 v[132:133], v[136:137], v[166:167], v[132:133] op_sel:[1,0,0]
	v_pk_fma_f32 v[126:127], v[122:123], v[196:197], v[126:127] op_sel_hi:[0,1,1]
	v_pk_mul_f32 v[146:147], v[128:129], v[128:129]
	v_cvt_pk_f32_fp8_e32 v[186:187], v188
	v_cvt_pk_f32_fp8_sdwa v[188:189], v188 src0_sel:WORD_1
	v_cvt_pk_f32_fp8_e32 v[190:191], v192
	v_cvt_pk_f32_fp8_sdwa v[192:193], v192 src0_sel:WORD_1
	v_pk_fma_f32 v[124:125], v[136:137], v[152:153], v[124:125] op_sel_hi:[0,1,1]
	v_pk_fma_f32 v[134:135], v[136:137], v[154:155], v[148:149] op_sel_hi:[0,1,1]
	v_pk_fma_f32 v[132:133], v[138:139], v[182:183], v[132:133] op_sel_hi:[0,1,1]
	v_pk_mul_f32 v[148:149], v[126:127], v[126:127]
	v_add_f32_e32 v131, v146, v147
	v_cvt_pk_f32_fp8_e32 v[202:203], v204
	v_cvt_pk_f32_fp8_sdwa v[204:205], v204 src0_sel:WORD_1
	v_cvt_pk_f32_fp8_e32 v[206:207], v208
	v_cvt_pk_f32_fp8_sdwa v[208:209], v208 src0_sel:WORD_1
	v_pk_fma_f32 v[124:125], v[136:137], v[168:169], v[124:125] op_sel:[1,0,0]
	v_pk_fma_f32 v[132:133], v[122:123], v[198:199], v[132:133] op_sel_hi:[0,1,1]
	v_add_f32_e32 v131, v131, v148
	v_pk_fma_f32 v[140:141], v[136:137], v[156:157], v[140:141] op_sel_hi:[0,1,1]
	v_pk_fma_f32 v[142:143], v[136:137], v[158:159], v[142:143] op_sel_hi:[0,1,1]
	v_pk_fma_f32 v[144:145], v[136:137], v[160:161], v[144:145] op_sel_hi:[0,1,1]
	v_pk_fma_f32 v[124:125], v[138:139], v[184:185], v[124:125] op_sel_hi:[0,1,1]
	v_pk_mul_f32 v[150:151], v[132:133], v[132:133]
	v_add_f32_e32 v131, v149, v131
	v_pk_fma_f32 v[140:141], v[136:137], v[172:173], v[140:141] op_sel:[1,0,0]
	v_pk_fma_f32 v[142:143], v[136:137], v[174:175], v[142:143] op_sel:[1,0,0]
	v_pk_fma_f32 v[144:145], v[136:137], v[176:177], v[144:145] op_sel:[1,0,0]
	v_pk_fma_f32 v[134:135], v[136:137], v[170:171], v[134:135] op_sel:[1,0,0]
	v_pk_fma_f32 v[124:125], v[122:123], v[200:201], v[124:125] op_sel_hi:[0,1,1]
	v_add_f32_e32 v131, v131, v150
	v_pk_fma_f32 v[136:137], v[138:139], v[188:189], v[140:141] op_sel_hi:[0,1,1]
	v_pk_fma_f32 v[140:141], v[138:139], v[190:191], v[142:143] op_sel_hi:[0,1,1]
	v_pk_fma_f32 v[142:143], v[138:139], v[192:193], v[144:145] op_sel_hi:[0,1,1]
	v_pk_fma_f32 v[134:135], v[138:139], v[186:187], v[134:135] op_sel_hi:[0,1,1]
	v_pk_mul_f32 v[152:153], v[124:125], v[124:125]
	v_add_f32_e32 v131, v151, v131
	v_pk_fma_f32 v[136:137], v[122:123], v[204:205], v[136:137] op_sel_hi:[0,1,1]
	v_pk_fma_f32 v[138:139], v[122:123], v[206:207], v[140:141] op_sel_hi:[0,1,1]
	v_pk_fma_f32 v[140:141], v[122:123], v[208:209], v[142:143] op_sel_hi:[0,1,1]
	v_pk_fma_f32 v[122:123], v[122:123], v[202:203], v[134:135] op_sel_hi:[0,1,1]
	v_add_f32_e32 v131, v152, v131
	v_pk_mul_f32 v[154:155], v[122:123], v[122:123]
	v_add_f32_e32 v131, v153, v131
	v_add_f32_e32 v131, v154, v131
	v_pk_mul_f32 v[134:135], v[136:137], v[136:137]
	v_add_f32_e32 v131, v155, v131
	v_add_f32_e32 v131, v134, v131
	v_pk_mul_f32 v[142:143], v[138:139], v[138:139]
	v_add_f32_e32 v131, v135, v131
	v_add_f32_e32 v131, v142, v131
	v_pk_mul_f32 v[144:145], v[140:141], v[140:141]
	v_add_f32_e32 v131, v143, v131
	v_add_f32_e32 v131, v144, v131
	v_add_f32_e32 v131, v145, v131
	s_nop 1
	v_add_f32_dpp v131, v131, v131 row_ror:1 row_mask:0xf bank_mask:0xf bound_ctrl:1
	s_nop 1
	v_add_f32_dpp v131, v131, v131 row_ror:2 row_mask:0xf bank_mask:0xf bound_ctrl:1
	s_nop 1
	v_add_f32_dpp v131, v131, v131 row_ror:4 row_mask:0xf bank_mask:0xf bound_ctrl:1
	s_nop 1
	v_add_f32_dpp v131, v131, v131 row_ror:8 row_mask:0xf bank_mask:0xf bound_ctrl:1
	s_nop 0
	v_readlane_b32 s31, v131, 16
	v_readlane_b32 s28, v131, 48
	v_readlane_b32 s36, v131, 0
	v_readlane_b32 s37, v131, 32
	v_mov_b32_e32 v134, s31
	v_mov_b32_e32 v135, s28
	v_pk_add_f32 v[134:135], s[36:37], v[134:135]
	s_nop 0
	v_add_f32_e32 v131, v134, v135
	v_fmamk_f32 v131, v131, 0x3a800000, v30
	v_mul_f32_e32 v134, 0x4b800000, v131
	v_cmp_gt_f32_e32 vcc, s3, v131
	s_nop 1
	v_cndmask_b32_e32 v131, v131, v134, vcc
	v_rsq_f32_e32 v131, v131
	s_nop 0
	v_mul_f32_e32 v134, 0x45800000, v131
	v_cndmask_b32_e32 v134, v131, v134, vcc
	v_pk_mul_f32 v[128:129], v[128:129], v[134:135] op_sel_hi:[1,0]
	v_pk_mul_f32 v[126:127], v[126:127], v[134:135] op_sel_hi:[1,0]
	v_pk_mul_f32 v[132:133], v[132:133], v[134:135] op_sel_hi:[1,0]
	v_pk_mul_f32 v[142:143], v[124:125], v[134:135] op_sel_hi:[1,0]
	v_pk_mul_f32 v[144:145], v[122:123], v[134:135] op_sel_hi:[1,0]
	v_pk_mul_f32 v[136:137], v[136:137], v[134:135] op_sel_hi:[1,0]
	v_pk_mul_f32 v[146:147], v[138:139], v[134:135] op_sel_hi:[1,0]
	v_pk_mul_f32 v[138:139], v[140:141], v[134:135] op_sel_hi:[1,0]
	v_pk_mul_f32 v[124:125], v[16:17], v[126:127]
	v_pk_mul_f32 v[122:123], v[14:15], v[128:129]
	v_pk_mul_f32 v[128:129], v[12:13], v[142:143]
	v_pk_mul_f32 v[126:127], v[10:11], v[132:133]
	v_pk_mul_f32 v[134:135], v[8:9], v[136:137]
	v_pk_mul_f32 v[132:133], v[6:7], v[144:145]
	v_pk_mul_f32 v[138:139], v[4:5], v[138:139]
	v_pk_mul_f32 v[136:137], v[2:3], v[146:147]
	global_store_dwordx4 v[118:119], v[122:125], off offset:-3072 nt
	global_store_dwordx4 v[118:119], v[126:129], off offset:-2048 nt
	global_store_dwordx4 v[118:119], v[132:135], off offset:-1024 nt
	global_store_dwordx4 v[118:119], v[136:139], off nt
	v_lshl_add_u64 v[0:1], v[118:119], 0, s[8:9]
	s_cmp_lt_i32 s0, 0x10000
	s_cbranch_scc1 .LBB0_1146
